# trailing half skips its last in-loop barrier and leading half drops the pre-epilogue alignment barrier in the up, down and in-proj fp8 GEMM loops
# speedup vs baseline: 1.0366x; 1.0366x over previous
.LBB0_217:
	ds_read_b128 v[18:21], v168
	ds_read_b128 v[22:25], v168 offset:1024
	ds_read_b128 v[26:29], v168 offset:2048
	ds_read_b128 v[30:33], v168 offset:3072
	ds_read_b128 v[2:5], v169
	ds_read_b128 v[6:9], v169 offset:1024
	ds_read_b128 v[10:13], v169 offset:2048
	ds_read_b128 v[14:17], v169 offset:3072
	s_add_u32 s78, s80, 0x100
	s_addc_u32 s79, s81, 0
	s_cmp_eq_u32 s33, 4
	s_cselect_b32 s86, s57, s78
	s_cselect_b32 s87, s7, s79
	s_cselect_b32 s84, vcc_lo, vcc_hi
	s_cselect_b32 s85, s59, s89
	s_add_u32 s82, s86, 0x80
	s_addc_u32 s83, s87, 0
	ds_read_b128 v[176:179], v170
	ds_read_b128 v[180:183], v170 offset:1024
	ds_read_b128 v[184:187], v170 offset:2048
	ds_read_b128 v[188:191], v170 offset:3072
	ds_read_b128 v[192:195], v170 offset:4096
	ds_read_b128 v[196:199], v170 offset:5120
	ds_read_b128 v[200:203], v170 offset:6144
	ds_read_b128 v[204:207], v170 offset:7168
	s_add_u32 s80, s80, 0x20080
	s_addc_u32 s81, s81, 0
	s_mov_b32 s29, m0
	s_mov_b32 m0, s91
	s_nop 2
	global_load_lds_dwordx4 v162, s[80:81]
	s_mov_b32 m0, s29
	s_nop 0
	s_mov_b32 s29, m0
	s_mov_b32 m0, s92
	s_nop 2
	global_load_lds_dwordx4 v164, s[80:81]
	s_mov_b32 m0, s29
	s_waitcnt vmcnt(8)
	s_waitcnt lgkmcnt(0)
	s_barrier
	s_setprio 1
	s_waitcnt lgkmcnt(6)
	v_mfma_f32_16x16x128_f8f6f4 v[158:161], v[18:25], v[176:183], v[158:161]
	v_mfma_f32_16x16x128_f8f6f4 v[154:157], v[26:33], v[176:183], v[154:157]
	s_waitcnt lgkmcnt(4)
	v_mfma_f32_16x16x128_f8f6f4 v[146:149], v[18:25], v[184:191], v[146:149]
	v_mfma_f32_16x16x128_f8f6f4 v[138:141], v[26:33], v[184:191], v[138:141]
	s_waitcnt lgkmcnt(2)
	v_mfma_f32_16x16x128_f8f6f4 v[130:133], v[18:25], v[192:199], v[130:133]
	v_mfma_f32_16x16x128_f8f6f4 v[122:125], v[26:33], v[192:199], v[122:125]
	s_waitcnt lgkmcnt(0)
	v_mfma_f32_16x16x128_f8f6f4 v[114:117], v[18:25], v[200:207], v[114:117]
	v_mfma_f32_16x16x128_f8f6f4 v[106:109], v[26:33], v[200:207], v[106:109]
	s_setprio 0
	s_setprio 1
	v_mfma_f32_16x16x128_f8f6f4 v[150:153], v[2:9], v[176:183], v[150:153]
	v_mfma_f32_16x16x128_f8f6f4 v[142:145], v[10:17], v[176:183], v[142:145]
	v_mfma_f32_16x16x128_f8f6f4 v[134:137], v[2:9], v[184:191], v[134:137]
	v_mfma_f32_16x16x128_f8f6f4 v[126:129], v[10:17], v[184:191], v[126:129]
	v_mfma_f32_16x16x128_f8f6f4 v[118:121], v[2:9], v[192:199], v[118:121]
	v_mfma_f32_16x16x128_f8f6f4 v[110:113], v[10:17], v[192:199], v[110:113]
	v_mfma_f32_16x16x128_f8f6f4 v[102:105], v[2:9], v[200:207], v[102:105]
	v_mfma_f32_16x16x128_f8f6f4 v[98:101], v[10:17], v[200:207], v[98:101]
	s_setprio 0
	s_barrier
	ds_read_b128 v[176:179], v170 offset:16384
	ds_read_b128 v[180:183], v170 offset:17408
	ds_read_b128 v[184:187], v170 offset:18432
	ds_read_b128 v[188:191], v170 offset:19456
	ds_read_b128 v[192:195], v170 offset:20480
	ds_read_b128 v[196:199], v170 offset:21504
	ds_read_b128 v[200:203], v170 offset:22528
	ds_read_b128 v[204:207], v170 offset:23552
	s_mov_b32 s29, m0
	s_mov_b32 m0, s36
	s_nop 2
	global_load_lds_dwordx4 v163, s[84:85]
	s_mov_b32 m0, s29
	s_add_u32 s80, s84, 0x20000
	s_mov_b32 s29, m0
	s_mov_b32 m0, s37
	s_nop 2
	global_load_lds_dwordx4 v165, s[84:85]
	s_mov_b32 m0, s29
	s_addc_u32 s81, s85, 0
	s_mov_b32 s29, m0
	s_mov_b32 m0, s55
	s_nop 2
	global_load_lds_dwordx4 v163, s[80:81]
	s_mov_b32 m0, s29
	s_nop 0
	s_mov_b32 s29, m0
	s_mov_b32 m0, s77
	s_nop 2
	global_load_lds_dwordx4 v165, s[80:81]
	s_mov_b32 m0, s29
	s_nop 0
	s_mov_b32 s29, m0
	s_mov_b32 m0, s35
	s_nop 2
	global_load_lds_dwordx4 v162, s[86:87]
	s_mov_b32 m0, s29
	s_nop 0
	s_mov_b32 s29, m0
	s_mov_b32 m0, s88
	s_nop 2
	global_load_lds_dwordx4 v164, s[86:87]
	s_mov_b32 m0, s29
	s_waitcnt vmcnt(8)
	s_waitcnt lgkmcnt(0)
	s_barrier
	s_setprio 1
	s_waitcnt lgkmcnt(6)
	v_mfma_f32_16x16x128_f8f6f4 v[94:97], v[18:25], v[176:183], v[94:97]
	v_mfma_f32_16x16x128_f8f6f4 v[90:93], v[26:33], v[176:183], v[90:93]
	s_waitcnt lgkmcnt(4)
	v_mfma_f32_16x16x128_f8f6f4 v[82:85], v[18:25], v[184:191], v[82:85]
	v_mfma_f32_16x16x128_f8f6f4 v[74:77], v[26:33], v[184:191], v[74:77]
	s_waitcnt lgkmcnt(2)
	v_mfma_f32_16x16x128_f8f6f4 v[66:69], v[18:25], v[192:199], v[66:69]
	v_mfma_f32_16x16x128_f8f6f4 v[58:61], v[26:33], v[192:199], v[58:61]
	s_waitcnt lgkmcnt(0)
	v_mfma_f32_16x16x128_f8f6f4 v[50:53], v[18:25], v[200:207], v[50:53]
	v_mfma_f32_16x16x128_f8f6f4 v[42:45], v[26:33], v[200:207], v[42:45]
	s_setprio 0
	s_setprio 1
	v_mfma_f32_16x16x128_f8f6f4 v[86:89], v[2:9], v[176:183], v[86:89]
	v_mfma_f32_16x16x128_f8f6f4 v[78:81], v[10:17], v[176:183], v[78:81]
	v_mfma_f32_16x16x128_f8f6f4 v[70:73], v[2:9], v[184:191], v[70:73]
	v_mfma_f32_16x16x128_f8f6f4 v[62:65], v[10:17], v[184:191], v[62:65]
	v_mfma_f32_16x16x128_f8f6f4 v[54:57], v[2:9], v[192:199], v[54:57]
	v_mfma_f32_16x16x128_f8f6f4 v[46:49], v[10:17], v[192:199], v[46:49]
	v_mfma_f32_16x16x128_f8f6f4 v[38:41], v[2:9], v[200:207], v[38:41]
	v_mfma_f32_16x16x128_f8f6f4 v[34:37], v[10:17], v[200:207], v[34:37]
	s_setprio 0
	s_barrier
	ds_read_b128 v[2:5], v172
	ds_read_b128 v[6:9], v172 offset:1024
	ds_read_b128 v[10:13], v172 offset:2048
	ds_read_b128 v[14:17], v172 offset:3072
	ds_read_b128 v[18:21], v174
	ds_read_b128 v[22:25], v174 offset:1024
	ds_read_b128 v[26:29], v174 offset:2048
	ds_read_b128 v[30:33], v174 offset:3072
	ds_read_b128 v[176:179], v170 offset:32768
	ds_read_b128 v[180:183], v170 offset:33792
	ds_read_b128 v[184:187], v170 offset:34816
	ds_read_b128 v[188:191], v170 offset:35840
	ds_read_b128 v[192:195], v170 offset:36864
	ds_read_b128 v[196:199], v170 offset:37888
	ds_read_b128 v[200:203], v170 offset:38912
	ds_read_b128 v[204:207], v170 offset:39936
	s_add_u32 s80, s86, 0x20000
	s_addc_u32 s81, s87, 0
	s_mov_b32 s29, m0
	s_mov_b32 m0, s97
	s_nop 2
	global_load_lds_dwordx4 v162, s[80:81]
	s_mov_b32 m0, s29
	s_nop 0
	s_mov_b32 s29, m0
	s_mov_b32 m0, s3
	s_nop 2
	global_load_lds_dwordx4 v164, s[80:81]
	s_mov_b32 m0, s29
	s_waitcnt vmcnt(8)
	s_waitcnt lgkmcnt(0)
	s_barrier
	s_setprio 1
	s_waitcnt lgkmcnt(6)
	v_mfma_f32_16x16x128_f8f6f4 v[158:161], v[2:9], v[176:183], v[158:161]
	v_mfma_f32_16x16x128_f8f6f4 v[154:157], v[10:17], v[176:183], v[154:157]
	s_waitcnt lgkmcnt(4)
	v_mfma_f32_16x16x128_f8f6f4 v[146:149], v[2:9], v[184:191], v[146:149]
	v_mfma_f32_16x16x128_f8f6f4 v[138:141], v[10:17], v[184:191], v[138:141]
	s_waitcnt lgkmcnt(2)
	v_mfma_f32_16x16x128_f8f6f4 v[130:133], v[2:9], v[192:199], v[130:133]
	v_mfma_f32_16x16x128_f8f6f4 v[122:125], v[10:17], v[192:199], v[122:125]
	s_waitcnt lgkmcnt(0)
	v_mfma_f32_16x16x128_f8f6f4 v[114:117], v[2:9], v[200:207], v[114:117]
	v_mfma_f32_16x16x128_f8f6f4 v[106:109], v[10:17], v[200:207], v[106:109]
	s_setprio 0
	s_setprio 1
	v_mfma_f32_16x16x128_f8f6f4 v[150:153], v[18:25], v[176:183], v[150:153]
	v_mfma_f32_16x16x128_f8f6f4 v[142:145], v[26:33], v[176:183], v[142:145]
	v_mfma_f32_16x16x128_f8f6f4 v[134:137], v[18:25], v[184:191], v[134:137]
	v_mfma_f32_16x16x128_f8f6f4 v[126:129], v[26:33], v[184:191], v[126:129]
	v_mfma_f32_16x16x128_f8f6f4 v[118:121], v[18:25], v[192:199], v[118:121]
	v_mfma_f32_16x16x128_f8f6f4 v[110:113], v[26:33], v[192:199], v[110:113]
	v_mfma_f32_16x16x128_f8f6f4 v[102:105], v[18:25], v[200:207], v[102:105]
	v_mfma_f32_16x16x128_f8f6f4 v[98:101], v[26:33], v[200:207], v[98:101]
	s_setprio 0
	s_barrier
	ds_read_b128 v[176:179], v170 offset:49152
	ds_read_b128 v[180:183], v170 offset:50176
	ds_read_b128 v[184:187], v170 offset:51200
	ds_read_b128 v[188:191], v170 offset:52224
	ds_read_b128 v[192:195], v170 offset:53248
	ds_read_b128 v[196:199], v170 offset:54272
	ds_read_b128 v[200:203], v170 offset:55296
	ds_read_b128 v[204:207], v170 offset:56320
	s_add_u32 s80, s84, 0x80
	s_addc_u32 s81, s85, 0
	s_mov_b32 s29, m0
	s_mov_b32 m0, s90
	s_nop 2
	global_load_lds_dwordx4 v163, s[80:81]
	s_mov_b32 m0, s29
	s_nop 0
	s_mov_b32 s29, m0
	s_mov_b32 m0, s28
	s_nop 2
	global_load_lds_dwordx4 v165, s[80:81]
	s_mov_b32 m0, s29
	s_add_u32 s80, s84, 0x20080
	s_addc_u32 s81, s85, 0
	s_mov_b32 s29, m0
	s_mov_b32 m0, s94
	s_nop 2
	global_load_lds_dwordx4 v163, s[80:81]
	s_mov_b32 m0, s29
	s_nop 0
	s_mov_b32 s29, m0
	s_mov_b32 m0, s95
	s_nop 2
	global_load_lds_dwordx4 v165, s[80:81]
	s_mov_b32 m0, s29
	s_nop 0
	s_mov_b32 s29, m0
	s_mov_b32 m0, s93
	s_nop 2
	global_load_lds_dwordx4 v162, s[82:83]
	s_mov_b32 m0, s29
	s_nop 0
	s_mov_b32 s29, m0
	s_mov_b32 m0, s2
	s_nop 2
	global_load_lds_dwordx4 v164, s[82:83]
	s_mov_b32 m0, s29
	s_waitcnt vmcnt(8)
	s_waitcnt lgkmcnt(0)
	s_barrier
	s_setprio 1
	s_waitcnt lgkmcnt(6)
	v_mfma_f32_16x16x128_f8f6f4 v[94:97], v[2:9], v[176:183], v[94:97]
	v_mfma_f32_16x16x128_f8f6f4 v[90:93], v[10:17], v[176:183], v[90:93]
	s_waitcnt lgkmcnt(4)
	v_mfma_f32_16x16x128_f8f6f4 v[82:85], v[2:9], v[184:191], v[82:85]
	v_mfma_f32_16x16x128_f8f6f4 v[74:77], v[10:17], v[184:191], v[74:77]
	s_waitcnt lgkmcnt(2)
	v_mfma_f32_16x16x128_f8f6f4 v[66:69], v[2:9], v[192:199], v[66:69]
	v_mfma_f32_16x16x128_f8f6f4 v[58:61], v[10:17], v[192:199], v[58:61]
	s_waitcnt lgkmcnt(0)
	v_mfma_f32_16x16x128_f8f6f4 v[50:53], v[2:9], v[200:207], v[50:53]
	v_mfma_f32_16x16x128_f8f6f4 v[42:45], v[10:17], v[200:207], v[42:45]
	s_setprio 0
	s_setprio 1
	v_mfma_f32_16x16x128_f8f6f4 v[86:89], v[18:25], v[176:183], v[86:89]
	v_mfma_f32_16x16x128_f8f6f4 v[78:81], v[26:33], v[176:183], v[78:81]
	v_mfma_f32_16x16x128_f8f6f4 v[70:73], v[18:25], v[184:191], v[70:73]
	v_mfma_f32_16x16x128_f8f6f4 v[62:65], v[26:33], v[184:191], v[62:65]
	v_mfma_f32_16x16x128_f8f6f4 v[54:57], v[18:25], v[192:199], v[54:57]
	v_mfma_f32_16x16x128_f8f6f4 v[46:49], v[26:33], v[192:199], v[46:49]
	v_mfma_f32_16x16x128_f8f6f4 v[38:41], v[18:25], v[200:207], v[38:41]
	v_mfma_f32_16x16x128_f8f6f4 v[34:37], v[26:33], v[200:207], v[34:37]
	s_setprio 0
	s_cmp_lt_i32 s33, 4
	s_cbranch_scc1 .Lkb1_do
	s_cmp_lg_u64 s[10:11], 0
	s_cbranch_scc0 .Lkb1_skip

.Lkb1_skip:
	s_add_i32 s33, s33, 2
	s_add_u32 vcc_hi, vcc_hi, 0x100
	s_addc_u32 s89, s89, 0
	s_cmp_gt_u32 s33, 5
	s_mov_b64 s[80:81], s[78:79]
	s_cbranch_scc0 .LBB0_217

.LBB0_1896:
	s_add_u32 s33, s74, s40
	s_addc_u32 s44, s75, s41
	s_add_u32 s56, s33, 0x1d800080
	s_addc_u32 s57, s44, 0
	s_add_u32 s33, s33, 0x1d800100
	s_addc_u32 s52, s44, 0
	v_add_u32_e32 v2, 0x10000, v173
	v_add_u32_e32 v14, 0x14000, v173
	s_and_b64 s[44:45], s[42:43], exec
	ds_read_b128 v[18:21], v2
	ds_read_b128 v[22:25], v2 offset:1024
	ds_read_b128 v[26:29], v2 offset:2048
	ds_read_b128 v[30:33], v2 offset:3072
	ds_read_b128 v[2:5], v14
	ds_read_b128 v[6:9], v14 offset:1024
	ds_read_b128 v[10:13], v14 offset:2048
	ds_read_b128 v[14:17], v14 offset:3072
	s_cselect_b32 s55, s11, s52
	s_cselect_b32 s54, s10, s33
	s_add_u32 s33, s2, s40
	s_addc_u32 s44, s23, s41
	s_and_b64 s[42:43], s[42:43], exec
	s_cselect_b32 s43, s39, s44
	s_cselect_b32 s42, s38, s33
	s_add_u32 s44, s54, 0x80
	s_addc_u32 s45, s55, 0
	s_add_u32 s52, s42, 0x80
	s_addc_u32 s53, s43, 0
	ds_read_b128 v[180:183], v174
	ds_read_b128 v[184:187], v174 offset:1024
	ds_read_b128 v[188:191], v174 offset:2048
	ds_read_b128 v[192:195], v174 offset:3072
	ds_read_b128 v[196:199], v174 offset:4096
	ds_read_b128 v[200:203], v174 offset:5120
	ds_read_b128 v[204:207], v174 offset:6144
	ds_read_b128 v[208:211], v174 offset:7168
	s_mov_b32 s33, m0
	s_mov_b32 m0, s93
	s_nop 2
	global_load_lds_dwordx4 v178, s[56:57]
	s_mov_b32 m0, s33
	s_nop 0
	s_mov_b32 s33, m0
	s_mov_b32 m0, s94
	s_nop 2
	global_load_lds_dwordx4 v177, s[56:57]
	s_mov_b32 m0, s33
	s_waitcnt vmcnt(8)
	s_waitcnt lgkmcnt(0)
	s_barrier
	s_setprio 1
	s_waitcnt lgkmcnt(6)
	v_mfma_f32_16x16x128_f8f6f4 v[158:161], v[18:25], v[180:187], v[158:161]
	v_mfma_f32_16x16x128_f8f6f4 v[154:157], v[26:33], v[180:187], v[154:157]
	s_waitcnt lgkmcnt(4)
	v_mfma_f32_16x16x128_f8f6f4 v[150:153], v[18:25], v[188:195], v[150:153]
	v_mfma_f32_16x16x128_f8f6f4 v[146:149], v[26:33], v[188:195], v[146:149]
	s_waitcnt lgkmcnt(2)
	v_mfma_f32_16x16x128_f8f6f4 v[142:145], v[18:25], v[196:203], v[142:145]
	v_mfma_f32_16x16x128_f8f6f4 v[138:141], v[26:33], v[196:203], v[138:141]
	s_waitcnt lgkmcnt(0)
	v_mfma_f32_16x16x128_f8f6f4 v[134:137], v[18:25], v[204:211], v[134:137]
	v_mfma_f32_16x16x128_f8f6f4 v[130:133], v[26:33], v[204:211], v[130:133]
	s_setprio 0
	s_setprio 1
	v_mfma_f32_16x16x128_f8f6f4 v[126:129], v[2:9], v[180:187], v[126:129]
	v_mfma_f32_16x16x128_f8f6f4 v[122:125], v[10:17], v[180:187], v[122:125]
	v_mfma_f32_16x16x128_f8f6f4 v[118:121], v[2:9], v[188:195], v[118:121]
	v_mfma_f32_16x16x128_f8f6f4 v[114:117], v[10:17], v[188:195], v[114:117]
	v_mfma_f32_16x16x128_f8f6f4 v[110:113], v[2:9], v[196:203], v[110:113]
	v_mfma_f32_16x16x128_f8f6f4 v[106:109], v[10:17], v[196:203], v[106:109]
	v_mfma_f32_16x16x128_f8f6f4 v[102:105], v[2:9], v[204:211], v[102:105]
	v_mfma_f32_16x16x128_f8f6f4 v[98:101], v[10:17], v[204:211], v[98:101]
	s_setprio 0
	s_barrier
	ds_read_b128 v[180:183], v174 offset:16384
	ds_read_b128 v[184:187], v174 offset:17408
	ds_read_b128 v[188:191], v174 offset:18432
	ds_read_b128 v[192:195], v174 offset:19456
	ds_read_b128 v[196:199], v174 offset:20480
	ds_read_b128 v[200:203], v174 offset:21504
	ds_read_b128 v[204:207], v174 offset:22528
	ds_read_b128 v[208:211], v174 offset:23552
	s_mov_b32 s33, m0
	s_mov_b32 m0, s67
	s_nop 2
	global_load_lds_dwordx4 v1, s[42:43]
	s_mov_b32 m0, s33
	s_add_u32 s56, s42, 0x20000
	s_mov_b32 s33, m0
	s_mov_b32 m0, s68
	s_nop 2
	global_load_lds_dwordx4 v163, s[42:43]
	s_mov_b32 m0, s33
	s_addc_u32 s57, s43, 0
	s_mov_b32 s33, m0
	s_mov_b32 m0, s69
	s_nop 2
	global_load_lds_dwordx4 v1, s[56:57]
	s_mov_b32 m0, s33
	s_nop 0
	s_mov_b32 s33, m0
	s_mov_b32 m0, s76
	s_nop 2
	global_load_lds_dwordx4 v163, s[56:57]
	s_mov_b32 m0, s33
	s_nop 0
	s_mov_b32 s33, m0
	s_mov_b32 m0, s15
	s_nop 2
	global_load_lds_dwordx4 v168, s[54:55]
	s_mov_b32 m0, s33
	s_nop 0
	s_mov_b32 s33, m0
	s_mov_b32 m0, s79
	s_nop 2
	global_load_lds_dwordx4 v172, s[54:55]
	s_mov_b32 m0, s33
	s_waitcnt vmcnt(8)
	s_waitcnt lgkmcnt(0)
	s_barrier
	s_setprio 1
	s_waitcnt lgkmcnt(6)
	v_mfma_f32_16x16x128_f8f6f4 v[94:97], v[18:25], v[180:187], v[94:97]
	v_mfma_f32_16x16x128_f8f6f4 v[90:93], v[26:33], v[180:187], v[90:93]
	s_waitcnt lgkmcnt(4)
	v_mfma_f32_16x16x128_f8f6f4 v[86:89], v[18:25], v[188:195], v[86:89]
	v_mfma_f32_16x16x128_f8f6f4 v[82:85], v[26:33], v[188:195], v[82:85]
	s_waitcnt lgkmcnt(2)
	v_mfma_f32_16x16x128_f8f6f4 v[78:81], v[18:25], v[196:203], v[78:81]
	v_mfma_f32_16x16x128_f8f6f4 v[74:77], v[26:33], v[196:203], v[74:77]
	s_waitcnt lgkmcnt(0)
	v_mfma_f32_16x16x128_f8f6f4 v[70:73], v[18:25], v[204:211], v[70:73]
	v_mfma_f32_16x16x128_f8f6f4 v[66:69], v[26:33], v[204:211], v[66:69]
	s_setprio 0
	s_setprio 1
	v_mfma_f32_16x16x128_f8f6f4 v[62:65], v[2:9], v[180:187], v[62:65]
	v_mfma_f32_16x16x128_f8f6f4 v[58:61], v[10:17], v[180:187], v[58:61]
	v_mfma_f32_16x16x128_f8f6f4 v[54:57], v[2:9], v[188:195], v[54:57]
	v_mfma_f32_16x16x128_f8f6f4 v[50:53], v[10:17], v[188:195], v[50:53]
	v_mfma_f32_16x16x128_f8f6f4 v[46:49], v[2:9], v[196:203], v[46:49]
	v_mfma_f32_16x16x128_f8f6f4 v[42:45], v[10:17], v[196:203], v[42:45]
	v_mfma_f32_16x16x128_f8f6f4 v[38:41], v[2:9], v[204:211], v[38:41]
	v_mfma_f32_16x16x128_f8f6f4 v[34:37], v[10:17], v[204:211], v[34:37]
	s_setprio 0
	s_barrier
	v_add_u32_e32 v14, 0x18000, v173
	v_add_u32_e32 v30, 0x1c000, v173
	ds_read_b128 v[2:5], v14
	ds_read_b128 v[6:9], v14 offset:1024
	ds_read_b128 v[10:13], v14 offset:2048
	ds_read_b128 v[14:17], v14 offset:3072
	ds_read_b128 v[18:21], v30
	ds_read_b128 v[22:25], v30 offset:1024
	ds_read_b128 v[26:29], v30 offset:2048
	ds_read_b128 v[30:33], v30 offset:3072
	ds_read_b128 v[180:183], v174 offset:32768
	ds_read_b128 v[184:187], v174 offset:33792
	ds_read_b128 v[188:191], v174 offset:34816
	ds_read_b128 v[192:195], v174 offset:35840
	ds_read_b128 v[196:199], v174 offset:36864
	ds_read_b128 v[200:203], v174 offset:37888
	ds_read_b128 v[204:207], v174 offset:38912
	ds_read_b128 v[208:211], v174 offset:39936
	s_mov_b32 s33, m0
	s_mov_b32 m0, s80
	s_nop 2
	global_load_lds_dwordx4 v169, s[54:55]
	s_mov_b32 m0, s33
	s_nop 0
	s_mov_b32 s33, m0
	s_mov_b32 m0, s81
	s_nop 2
	global_load_lds_dwordx4 v175, s[54:55]
	s_mov_b32 m0, s33
	s_waitcnt vmcnt(8)
	s_waitcnt lgkmcnt(0)
	s_barrier
	s_setprio 1
	s_waitcnt lgkmcnt(6)
	v_mfma_f32_16x16x128_f8f6f4 v[158:161], v[2:9], v[180:187], v[158:161]
	v_mfma_f32_16x16x128_f8f6f4 v[154:157], v[10:17], v[180:187], v[154:157]
	s_waitcnt lgkmcnt(4)
	v_mfma_f32_16x16x128_f8f6f4 v[150:153], v[2:9], v[188:195], v[150:153]
	v_mfma_f32_16x16x128_f8f6f4 v[146:149], v[10:17], v[188:195], v[146:149]
	s_waitcnt lgkmcnt(2)
	v_mfma_f32_16x16x128_f8f6f4 v[142:145], v[2:9], v[196:203], v[142:145]
	v_mfma_f32_16x16x128_f8f6f4 v[138:141], v[10:17], v[196:203], v[138:141]
	s_waitcnt lgkmcnt(0)
	v_mfma_f32_16x16x128_f8f6f4 v[134:137], v[2:9], v[204:211], v[134:137]
	v_mfma_f32_16x16x128_f8f6f4 v[130:133], v[10:17], v[204:211], v[130:133]
	s_setprio 0
	s_setprio 1
	v_mfma_f32_16x16x128_f8f6f4 v[126:129], v[18:25], v[180:187], v[126:129]
	v_mfma_f32_16x16x128_f8f6f4 v[122:125], v[26:33], v[180:187], v[122:125]
	v_mfma_f32_16x16x128_f8f6f4 v[118:121], v[18:25], v[188:195], v[118:121]
	v_mfma_f32_16x16x128_f8f6f4 v[114:117], v[26:33], v[188:195], v[114:117]
	v_mfma_f32_16x16x128_f8f6f4 v[110:113], v[18:25], v[196:203], v[110:113]
	v_mfma_f32_16x16x128_f8f6f4 v[106:109], v[26:33], v[196:203], v[106:109]
	v_mfma_f32_16x16x128_f8f6f4 v[102:105], v[18:25], v[204:211], v[102:105]
	v_mfma_f32_16x16x128_f8f6f4 v[98:101], v[26:33], v[204:211], v[98:101]
	s_setprio 0
	s_barrier
	ds_read_b128 v[180:183], v174 offset:49152
	ds_read_b128 v[184:187], v174 offset:50176
	ds_read_b128 v[188:191], v174 offset:51200
	ds_read_b128 v[192:195], v174 offset:52224
	ds_read_b128 v[196:199], v174 offset:53248
	ds_read_b128 v[200:203], v174 offset:54272
	ds_read_b128 v[204:207], v174 offset:55296
	ds_read_b128 v[208:211], v174 offset:56320
	s_mov_b32 s33, m0
	s_mov_b32 m0, s84
	s_nop 2
	global_load_lds_dwordx4 v1, s[52:53]
	s_mov_b32 m0, s33
	s_add_u32 s42, s42, 0x20080
	s_mov_b32 s33, m0
	s_mov_b32 m0, s85
	s_nop 2
	global_load_lds_dwordx4 v163, s[52:53]
	s_mov_b32 m0, s33
	s_addc_u32 s43, s43, 0
	s_mov_b32 s33, m0
	s_mov_b32 m0, s91
	s_nop 2
	global_load_lds_dwordx4 v1, s[42:43]
	s_mov_b32 m0, s33
	s_nop 0
	s_mov_b32 s33, m0
	s_mov_b32 m0, s92
	s_nop 2
	global_load_lds_dwordx4 v163, s[42:43]
	s_mov_b32 m0, s33
	s_nop 0
	s_mov_b32 s33, m0
	s_mov_b32 m0, s86
	s_nop 2
	global_load_lds_dwordx4 v168, s[44:45]
	s_mov_b32 m0, s33
	s_nop 0
	s_mov_b32 s33, m0
	s_mov_b32 m0, s87
	s_nop 2
	global_load_lds_dwordx4 v172, s[44:45]
	s_mov_b32 m0, s33
	s_waitcnt vmcnt(8)
	s_waitcnt lgkmcnt(0)
	s_barrier
	s_setprio 1
	s_waitcnt lgkmcnt(6)
	v_mfma_f32_16x16x128_f8f6f4 v[94:97], v[2:9], v[180:187], v[94:97]
	v_mfma_f32_16x16x128_f8f6f4 v[90:93], v[10:17], v[180:187], v[90:93]
	s_waitcnt lgkmcnt(4)
	v_mfma_f32_16x16x128_f8f6f4 v[86:89], v[2:9], v[188:195], v[86:89]
	v_mfma_f32_16x16x128_f8f6f4 v[82:85], v[10:17], v[188:195], v[82:85]
	s_waitcnt lgkmcnt(2)
	v_mfma_f32_16x16x128_f8f6f4 v[78:81], v[2:9], v[196:203], v[78:81]
	v_mfma_f32_16x16x128_f8f6f4 v[74:77], v[10:17], v[196:203], v[74:77]
	s_waitcnt lgkmcnt(0)
	v_mfma_f32_16x16x128_f8f6f4 v[70:73], v[2:9], v[204:211], v[70:73]
	v_mfma_f32_16x16x128_f8f6f4 v[66:69], v[10:17], v[204:211], v[66:69]
	s_setprio 0
	s_setprio 1
	v_mfma_f32_16x16x128_f8f6f4 v[62:65], v[18:25], v[180:187], v[62:65]
	v_mfma_f32_16x16x128_f8f6f4 v[58:61], v[26:33], v[180:187], v[58:61]
	v_mfma_f32_16x16x128_f8f6f4 v[54:57], v[18:25], v[188:195], v[54:57]
	v_mfma_f32_16x16x128_f8f6f4 v[50:53], v[26:33], v[188:195], v[50:53]
	v_mfma_f32_16x16x128_f8f6f4 v[46:49], v[18:25], v[196:203], v[46:49]
	v_mfma_f32_16x16x128_f8f6f4 v[42:45], v[26:33], v[196:203], v[42:45]
	v_mfma_f32_16x16x128_f8f6f4 v[38:41], v[18:25], v[204:211], v[38:41]
	v_mfma_f32_16x16x128_f8f6f4 v[34:37], v[26:33], v[204:211], v[34:37]
	s_setprio 0
	s_cmp_lt_i32 s9, 4
	s_cbranch_scc1 .Lkb6_do
	s_cmp_lg_u64 s[16:17], 0
	s_cbranch_scc0 .Lkb6_skip

.Lkb6_skip:
	s_add_u32 s40, s40, 0x100
	s_addc_u32 s41, s41, 0
	s_add_i32 s9, s9, 2
	s_cmp_gt_u32 s9, 5
	s_cbranch_scc1 .LBB0_1909

.LBB0_1909:
.LBB0_1911:
	s_cmp_lt_i32 s88, 1
	v_readlane_b32 s90, v253, 26
	s_cbranch_scc1 .LBB0_1916
	s_waitcnt vmcnt(8)
	s_and_saveexec_b64 s[40:41], s[4:5]
	s_cbranch_execz .LBB0_1915
	s_mov_b64 s[42:43], exec
	v_mbcnt_lo_u32_b32 v2, s42, 0
	v_mbcnt_hi_u32_b32 v2, s43, v2
	v_cmp_eq_u32_e32 vcc, 0, v2
	s_and_b64 s[8:9], exec, vcc
	s_mov_b64 exec, s[8:9]
	s_cbranch_execz .LBB0_1915
	s_lshl_b32 s8, s30, 6
	s_ashr_i32 s9, s8, 31
	s_lshl_b64 s[8:9], s[8:9], 2
	v_readlane_b32 s25, v253, 8
	s_add_u32 s8, s25, s8
	v_readlane_b32 s25, v253, 31
	s_addc_u32 s9, s25, s9
	s_bcnt1_i32_b64 s25, s[42:43]
	v_mov_b32_e32 v2, s25
	global_atomic_add v171, v2, s[8:9]

.LBB0_2092:
	s_lshl_b32 s33, s91, 7
	s_add_u32 s52, s36, s33
	s_addc_u32 s53, s37, 0
	s_add_u32 s46, s52, 0x100
	s_addc_u32 s47, s53, 0
	s_and_b64 s[44:45], s[42:43], exec
	s_cselect_b32 s49, s15, s47
	s_cselect_b32 s48, s17, s46
	s_add_u32 s33, s26, s33
	v_add_u32_e32 v2, 0x10000, v171
	v_add_u32_e32 v14, 0x14000, v171
	s_addc_u32 s44, s27, 0
	ds_read_b128 v[18:21], v2
	ds_read_b128 v[22:25], v2 offset:1024
	ds_read_b128 v[26:29], v2 offset:2048
	ds_read_b128 v[30:33], v2 offset:3072
	ds_read_b128 v[2:5], v14
	ds_read_b128 v[6:9], v14 offset:1024
	ds_read_b128 v[10:13], v14 offset:2048
	ds_read_b128 v[14:17], v14 offset:3072
	s_add_u32 s33, s33, 0x100
	s_addc_u32 s44, s44, 0
	s_and_b64 s[42:43], s[42:43], exec
	s_cselect_b32 s43, s19, s44
	s_cselect_b32 s42, s18, s33
	s_add_u32 s44, s48, 0x80
	s_addc_u32 s45, s49, 0
	s_add_u32 s46, s42, 0x80
	s_addc_u32 s47, s43, 0
	ds_read_b128 v[176:179], v172
	ds_read_b128 v[180:183], v172 offset:1024
	ds_read_b128 v[184:187], v172 offset:2048
	ds_read_b128 v[188:191], v172 offset:3072
	ds_read_b128 v[192:195], v172 offset:4096
	ds_read_b128 v[196:199], v172 offset:5120
	ds_read_b128 v[200:203], v172 offset:6144
	ds_read_b128 v[204:207], v172 offset:7168
	s_add_u32 s52, s52, 0x20080
	s_addc_u32 s53, s53, 0
	s_mov_b32 s33, m0
	s_mov_b32 m0, s79
	s_nop 2
	global_load_lds_dwordx4 v163, s[52:53]
	s_mov_b32 m0, s33
	s_nop 0
	s_mov_b32 s33, m0
	s_mov_b32 m0, s80
	s_nop 2
	global_load_lds_dwordx4 v164, s[52:53]
	s_mov_b32 m0, s33
	s_waitcnt vmcnt(8)
	s_waitcnt lgkmcnt(0)
	s_barrier
	s_setprio 1
	s_waitcnt lgkmcnt(6)
	v_mfma_f32_16x16x128_f8f6f4 v[158:161], v[18:25], v[176:183], v[158:161]
	v_mfma_f32_16x16x128_f8f6f4 v[154:157], v[26:33], v[176:183], v[154:157]
	s_waitcnt lgkmcnt(4)
	v_mfma_f32_16x16x128_f8f6f4 v[142:145], v[18:25], v[184:191], v[142:145]
	v_mfma_f32_16x16x128_f8f6f4 v[138:141], v[26:33], v[184:191], v[138:141]
	s_waitcnt lgkmcnt(2)
	v_mfma_f32_16x16x128_f8f6f4 v[126:129], v[18:25], v[192:199], v[126:129]
	v_mfma_f32_16x16x128_f8f6f4 v[122:125], v[26:33], v[192:199], v[122:125]
	s_waitcnt lgkmcnt(0)
	v_mfma_f32_16x16x128_f8f6f4 v[110:113], v[18:25], v[200:207], v[110:113]
	v_mfma_f32_16x16x128_f8f6f4 v[106:109], v[26:33], v[200:207], v[106:109]
	s_setprio 0
	s_setprio 1
	v_mfma_f32_16x16x128_f8f6f4 v[150:153], v[2:9], v[176:183], v[150:153]
	v_mfma_f32_16x16x128_f8f6f4 v[146:149], v[10:17], v[176:183], v[146:149]
	v_mfma_f32_16x16x128_f8f6f4 v[134:137], v[2:9], v[184:191], v[134:137]
	v_mfma_f32_16x16x128_f8f6f4 v[130:133], v[10:17], v[184:191], v[130:133]
	v_mfma_f32_16x16x128_f8f6f4 v[118:121], v[2:9], v[192:199], v[118:121]
	v_mfma_f32_16x16x128_f8f6f4 v[114:117], v[10:17], v[192:199], v[114:117]
	v_mfma_f32_16x16x128_f8f6f4 v[102:105], v[2:9], v[200:207], v[102:105]
	v_mfma_f32_16x16x128_f8f6f4 v[98:101], v[10:17], v[200:207], v[98:101]
	s_setprio 0
	s_barrier
	ds_read_b128 v[176:179], v172 offset:16384
	ds_read_b128 v[180:183], v172 offset:17408
	ds_read_b128 v[184:187], v172 offset:18432
	ds_read_b128 v[188:191], v172 offset:19456
	ds_read_b128 v[192:195], v172 offset:20480
	ds_read_b128 v[196:199], v172 offset:21504
	ds_read_b128 v[200:203], v172 offset:22528
	ds_read_b128 v[204:207], v172 offset:23552
	s_mov_b32 s33, m0
	s_mov_b32 m0, s64
	s_nop 2
	global_load_lds_dwordx4 v1, s[42:43]
	s_mov_b32 m0, s33
	s_add_u32 s52, s42, 0x20000
	s_mov_b32 s33, m0
	s_mov_b32 m0, s65
	s_nop 2
	global_load_lds_dwordx4 v162, s[42:43]
	s_mov_b32 m0, s33
	s_addc_u32 s53, s43, 0
	s_mov_b32 s33, m0
	s_mov_b32 m0, s24
	s_nop 2
	global_load_lds_dwordx4 v1, s[52:53]
	s_mov_b32 m0, s33
	s_nop 0
	s_mov_b32 s33, m0
	s_mov_b32 m0, s25
	s_nop 2
	global_load_lds_dwordx4 v162, s[52:53]
	s_mov_b32 m0, s33
	s_nop 0
	s_mov_b32 s33, m0
	s_mov_b32 m0, s63
	s_nop 2
	global_load_lds_dwordx4 v163, s[48:49]
	s_mov_b32 m0, s33
	s_nop 0
	s_mov_b32 s33, m0
	s_mov_b32 m0, s2
	s_nop 2
	global_load_lds_dwordx4 v164, s[48:49]
	s_mov_b32 m0, s33
	s_waitcnt vmcnt(8)
	s_waitcnt lgkmcnt(0)
	s_barrier
	s_setprio 1
	s_waitcnt lgkmcnt(6)
	v_mfma_f32_16x16x128_f8f6f4 v[94:97], v[18:25], v[176:183], v[94:97]
	v_mfma_f32_16x16x128_f8f6f4 v[90:93], v[26:33], v[176:183], v[90:93]
	s_waitcnt lgkmcnt(4)
	v_mfma_f32_16x16x128_f8f6f4 v[78:81], v[18:25], v[184:191], v[78:81]
	v_mfma_f32_16x16x128_f8f6f4 v[74:77], v[26:33], v[184:191], v[74:77]
	s_waitcnt lgkmcnt(2)
	v_mfma_f32_16x16x128_f8f6f4 v[62:65], v[18:25], v[192:199], v[62:65]
	v_mfma_f32_16x16x128_f8f6f4 v[58:61], v[26:33], v[192:199], v[58:61]
	s_waitcnt lgkmcnt(0)
	v_mfma_f32_16x16x128_f8f6f4 v[46:49], v[18:25], v[200:207], v[46:49]
	v_mfma_f32_16x16x128_f8f6f4 v[42:45], v[26:33], v[200:207], v[42:45]
	s_setprio 0
	s_setprio 1
	v_mfma_f32_16x16x128_f8f6f4 v[86:89], v[2:9], v[176:183], v[86:89]
	v_mfma_f32_16x16x128_f8f6f4 v[82:85], v[10:17], v[176:183], v[82:85]
	v_mfma_f32_16x16x128_f8f6f4 v[70:73], v[2:9], v[184:191], v[70:73]
	v_mfma_f32_16x16x128_f8f6f4 v[66:69], v[10:17], v[184:191], v[66:69]
	v_mfma_f32_16x16x128_f8f6f4 v[54:57], v[2:9], v[192:199], v[54:57]
	v_mfma_f32_16x16x128_f8f6f4 v[50:53], v[10:17], v[192:199], v[50:53]
	v_mfma_f32_16x16x128_f8f6f4 v[38:41], v[2:9], v[200:207], v[38:41]
	v_mfma_f32_16x16x128_f8f6f4 v[34:37], v[10:17], v[200:207], v[34:37]
	s_setprio 0
	s_barrier
	v_add_u32_e32 v14, 0x18000, v171
	v_add_u32_e32 v30, 0x1c000, v171
	ds_read_b128 v[2:5], v14
	ds_read_b128 v[6:9], v14 offset:1024
	ds_read_b128 v[10:13], v14 offset:2048
	ds_read_b128 v[14:17], v14 offset:3072
	ds_read_b128 v[18:21], v30
	ds_read_b128 v[22:25], v30 offset:1024
	ds_read_b128 v[26:29], v30 offset:2048
	ds_read_b128 v[30:33], v30 offset:3072
	ds_read_b128 v[176:179], v172 offset:32768
	ds_read_b128 v[180:183], v172 offset:33792
	ds_read_b128 v[184:187], v172 offset:34816
	ds_read_b128 v[188:191], v172 offset:35840
	ds_read_b128 v[192:195], v172 offset:36864
	ds_read_b128 v[196:199], v172 offset:37888
	ds_read_b128 v[200:203], v172 offset:38912
	ds_read_b128 v[204:207], v172 offset:39936
	s_add_u32 s48, s48, 0x20000
	s_addc_u32 s49, s49, 0
	s_mov_b32 s33, m0
	s_mov_b32 m0, s23
	s_nop 2
	global_load_lds_dwordx4 v163, s[48:49]
	s_mov_b32 m0, s33
	s_nop 0
	s_mov_b32 s33, m0
	s_mov_b32 m0, s28
	s_nop 2
	global_load_lds_dwordx4 v164, s[48:49]
	s_mov_b32 m0, s33
	s_waitcnt vmcnt(8)
	s_waitcnt lgkmcnt(0)
	s_barrier
	s_setprio 1
	s_waitcnt lgkmcnt(6)
	v_mfma_f32_16x16x128_f8f6f4 v[158:161], v[2:9], v[176:183], v[158:161]
	v_mfma_f32_16x16x128_f8f6f4 v[154:157], v[10:17], v[176:183], v[154:157]
	s_waitcnt lgkmcnt(4)
	v_mfma_f32_16x16x128_f8f6f4 v[142:145], v[2:9], v[184:191], v[142:145]
	v_mfma_f32_16x16x128_f8f6f4 v[138:141], v[10:17], v[184:191], v[138:141]
	s_waitcnt lgkmcnt(2)
	v_mfma_f32_16x16x128_f8f6f4 v[126:129], v[2:9], v[192:199], v[126:129]
	v_mfma_f32_16x16x128_f8f6f4 v[122:125], v[10:17], v[192:199], v[122:125]
	s_waitcnt lgkmcnt(0)
	v_mfma_f32_16x16x128_f8f6f4 v[110:113], v[2:9], v[200:207], v[110:113]
	v_mfma_f32_16x16x128_f8f6f4 v[106:109], v[10:17], v[200:207], v[106:109]
	s_setprio 0
	s_setprio 1
	v_mfma_f32_16x16x128_f8f6f4 v[150:153], v[18:25], v[176:183], v[150:153]
	v_mfma_f32_16x16x128_f8f6f4 v[146:149], v[26:33], v[176:183], v[146:149]
	v_mfma_f32_16x16x128_f8f6f4 v[134:137], v[18:25], v[184:191], v[134:137]
	v_mfma_f32_16x16x128_f8f6f4 v[130:133], v[26:33], v[184:191], v[130:133]
	v_mfma_f32_16x16x128_f8f6f4 v[118:121], v[18:25], v[192:199], v[118:121]
	v_mfma_f32_16x16x128_f8f6f4 v[114:117], v[26:33], v[192:199], v[114:117]
	v_mfma_f32_16x16x128_f8f6f4 v[102:105], v[18:25], v[200:207], v[102:105]
	v_mfma_f32_16x16x128_f8f6f4 v[98:101], v[26:33], v[200:207], v[98:101]
	s_setprio 0
	s_barrier
	ds_read_b128 v[176:179], v172 offset:49152
	ds_read_b128 v[180:183], v172 offset:50176
	ds_read_b128 v[184:187], v172 offset:51200
	ds_read_b128 v[188:191], v172 offset:52224
	ds_read_b128 v[192:195], v172 offset:53248
	ds_read_b128 v[196:199], v172 offset:54272
	ds_read_b128 v[200:203], v172 offset:55296
	ds_read_b128 v[204:207], v172 offset:56320
	s_mov_b32 s33, m0
	s_mov_b32 m0, s67
	s_nop 2
	global_load_lds_dwordx4 v1, s[46:47]
	s_mov_b32 m0, s33
	s_add_u32 s42, s42, 0x20080
	s_mov_b32 s33, m0
	s_mov_b32 m0, s68
	s_nop 2
	global_load_lds_dwordx4 v162, s[46:47]
	s_mov_b32 m0, s33
	s_addc_u32 s43, s43, 0
	s_mov_b32 s33, m0
	s_mov_b32 m0, s77
	s_nop 2
	global_load_lds_dwordx4 v1, s[42:43]
	s_mov_b32 m0, s33
	s_nop 0
	s_mov_b32 s33, m0
	s_mov_b32 m0, s78
	s_nop 2
	global_load_lds_dwordx4 v162, s[42:43]
	s_mov_b32 m0, s33
	s_nop 0
	s_mov_b32 s33, m0
	s_mov_b32 m0, s69
	s_nop 2
	global_load_lds_dwordx4 v163, s[44:45]
	s_mov_b32 m0, s33
	s_nop 0
	s_mov_b32 s33, m0
	s_mov_b32 m0, s76
	s_nop 2
	global_load_lds_dwordx4 v164, s[44:45]
	s_mov_b32 m0, s33
	s_waitcnt vmcnt(8)
	s_waitcnt lgkmcnt(0)
	s_barrier
	s_setprio 1
	s_waitcnt lgkmcnt(6)
	v_mfma_f32_16x16x128_f8f6f4 v[94:97], v[2:9], v[176:183], v[94:97]
	v_mfma_f32_16x16x128_f8f6f4 v[90:93], v[10:17], v[176:183], v[90:93]
	s_waitcnt lgkmcnt(4)
	v_mfma_f32_16x16x128_f8f6f4 v[78:81], v[2:9], v[184:191], v[78:81]
	v_mfma_f32_16x16x128_f8f6f4 v[74:77], v[10:17], v[184:191], v[74:77]
	s_waitcnt lgkmcnt(2)
	v_mfma_f32_16x16x128_f8f6f4 v[62:65], v[2:9], v[192:199], v[62:65]
	v_mfma_f32_16x16x128_f8f6f4 v[58:61], v[10:17], v[192:199], v[58:61]
	s_waitcnt lgkmcnt(0)
	v_mfma_f32_16x16x128_f8f6f4 v[46:49], v[2:9], v[200:207], v[46:49]
	v_mfma_f32_16x16x128_f8f6f4 v[42:45], v[10:17], v[200:207], v[42:45]
	s_setprio 0
	s_setprio 1
	v_mfma_f32_16x16x128_f8f6f4 v[86:89], v[18:25], v[176:183], v[86:89]
	v_mfma_f32_16x16x128_f8f6f4 v[82:85], v[26:33], v[176:183], v[82:85]
	v_mfma_f32_16x16x128_f8f6f4 v[70:73], v[18:25], v[184:191], v[70:73]
	v_mfma_f32_16x16x128_f8f6f4 v[66:69], v[26:33], v[184:191], v[66:69]
	v_mfma_f32_16x16x128_f8f6f4 v[54:57], v[18:25], v[192:199], v[54:57]
	v_mfma_f32_16x16x128_f8f6f4 v[50:53], v[26:33], v[192:199], v[50:53]
	v_mfma_f32_16x16x128_f8f6f4 v[38:41], v[18:25], v[200:207], v[38:41]
	v_mfma_f32_16x16x128_f8f6f4 v[34:37], v[26:33], v[200:207], v[34:37]
	s_setprio 0
	s_cmp_lt_u32 s91, 6
	s_cbranch_scc1 .Lkb7_do
	s_cmp_lg_u64 s[12:13], 0
	s_cbranch_scc0 .Lkb7_skip

.Lkb7_skip:
	s_add_i32 s33, s91, 2
	s_cmp_gt_u32 s91, 5
	s_cbranch_scc1 .LBB0_2094
	s_mov_b32 s91, s33
	s_cmp_eq_u32 s91, 6
	s_cselect_b64 s[42:43], -1, 0
	s_and_b64 vcc, exec, s[6:7]
	s_cbranch_vccz .LBB0_2063
	s_branch .LBB0_2084
.LBB0_2094:
.LBB0_2096:
	s_nop 15
	s_nop 15
	v_mov_b32_e32 v2, v166
	v_mov_b32_e32 v3, v165
	v_mov_b32_e32 v4, s39
	ds_read_b32 v4, v4 offset:288
	s_lshl_b32 s15, s85, 11
	v_lshlrev_b32_e32 v18, 3, v2
	s_add_i32 s15, s15, 0
	s_add_i32 s15, s15, 0x21000
	v_add_u32_e32 v2, s66, v18
	v_lshl_add_u32 v8, v2, 2, s15
	ds_read_b128 v[10:13], v8
	s_waitcnt lgkmcnt(1)
	v_readfirstlane_b32 s17, v4
	s_lshl_b32 s17, s17, 2
	s_add_i32 s17, s17, 0
	s_add_i32 s17, s17, 0x201c0
	v_mov_b32_e32 v2, s17
	ds_read2_b32 v[6:7], v2 offset1:32
	v_add_u32_e32 v19, s29, v3
	v_add_u32_e32 v21, 16, v19
	v_add_u32_e32 v23, 32, v19
	v_lshl_add_u32 v22, v21, 2, s15
	s_waitcnt lgkmcnt(0)
	v_readfirstlane_b32 s17, v7
	s_sub_i32 s17, s22, s17
	v_readfirstlane_b32 s26, v6
	v_lshl_add_u32 v6, v19, 2, s15
	v_lshl_add_u32 v24, v23, 2, s15
	ds_read_b128 v[14:17], v8 offset:16
	ds_read_b128 v[2:5], v8 offset:512
	s_lshl_b32 s17, s17, 8
	ds_read_b32 v25, v6 offset:1024
	ds_read_b128 v[6:9], v8 offset:528
	ds_read_b32 v22, v22 offset:1024
	ds_read_b32 v24, v24 offset:1024
	v_add_u32_e32 v20, s17, v19
	v_cmp_gt_i32_e32 vcc, s26, v20
	v_add_u32_e32 v20, s17, v21
	v_add_u32_e32 v27, 0xa0, v19
	s_waitcnt lgkmcnt(3)
	v_cndmask_b32_e32 v176, 0, v25, vcc
	v_cmp_gt_i32_e32 vcc, s26, v20
	v_add_u32_e32 v20, s17, v23
	v_add_u32_e32 v29, 0xb0, v19
	s_waitcnt lgkmcnt(1)
	v_cndmask_b32_e32 v178, 0, v22, vcc
	v_cmp_gt_i32_e32 vcc, s26, v20
	v_add_u32_e32 v20, 48, v19
	v_add_u32_e32 v22, 0x80, v19
	s_waitcnt lgkmcnt(0)
	v_cndmask_b32_e32 v32, 0, v24, vcc
	v_add_u32_e32 v24, 0x90, v19
	v_lshl_add_u32 v21, v20, 2, s15
	v_add_u32_e32 v20, s17, v20
	v_lshl_add_u32 v23, v22, 2, s15
	v_lshl_add_u32 v25, v24, 2, s15
	v_lshl_add_u32 v26, v27, 2, s15
	v_lshl_add_u32 v28, v29, 2, s15
	ds_read_b32 v21, v21 offset:1024
	ds_read_b32 v23, v23 offset:1024
	ds_read_b32 v25, v25 offset:1024
	ds_read_b32 v31, v26 offset:1024
	ds_read_b32 v33, v28 offset:1024
	v_cmp_gt_i32_e32 vcc, s26, v20
	v_add_u32_e32 v20, s17, v22
	v_mul_f32_e32 v180, 0x3b800000, v176
	s_waitcnt lgkmcnt(4)
	v_cndmask_b32_e32 v30, 0, v21, vcc
	v_cmp_gt_i32_e32 vcc, s26, v20
	v_lshl_add_u32 v22, s22, 8, v19
	v_pk_mul_f32 v[158:159], v[158:159], v[180:181] op_sel_hi:[1,0]
	s_waitcnt lgkmcnt(3)
	v_cndmask_b32_e32 v28, 0, v23, vcc
	v_add_u32_e32 v20, s17, v24
	v_ashrrev_i32_e32 v23, 31, v22
	v_pk_fma_f32 v[158:159], v[10:11], v[176:177], v[158:159] op_sel_hi:[1,0,1]
	v_pk_mul_f32 v[154:155], v[154:155], v[180:181] op_sel_hi:[1,0]
	v_cmp_gt_i32_e32 vcc, s26, v20
	v_lshlrev_b64 v[182:183], 10, v[22:23]
	v_pk_fma_f32 v[154:155], v[14:15], v[176:177], v[154:155] op_sel_hi:[1,0,1]
	v_med3_f32 v21, v158, s83, v173
	v_med3_f32 v23, v159, s83, v173
	v_mov_b32_e32 v158, 0
	s_waitcnt lgkmcnt(2)
	v_cndmask_b32_e32 v26, 0, v25, vcc
	v_add_u32_e32 v20, s17, v27
	v_cvt_pk_fp8_f32 v158, v21, v23
	v_med3_f32 v25, v154, s83, v173
	v_med3_f32 v27, v155, s83, v173
	v_mov_b32_e32 v159, 0
	v_pk_mul_f32 v[160:161], v[160:161], v[180:181] op_sel_hi:[1,0]
	v_cvt_pk_fp8_f32 v159, v25, v27
	v_pk_fma_f32 v[160:161], v[12:13], v[176:177], v[160:161] op_sel_hi:[1,0,1]
	v_pk_mul_f32 v[156:157], v[156:157], v[180:181] op_sel_hi:[1,0]
	v_med3_f32 v21, v160, s83, v173
	v_pk_fma_f32 v[156:157], v[16:17], v[176:177], v[156:157] op_sel_hi:[1,0,1]
	v_med3_f32 v23, v161, s83, v173
	v_pk_mul_f32 v[150:151], v[150:151], v[180:181] op_sel_hi:[1,0]
	v_cvt_pk_fp8_f32 v158, v21, v23 op_sel:[0,0,1]
	v_med3_f32 v21, v156, s83, v173
	v_med3_f32 v23, v157, s83, v173
	v_pk_fma_f32 v[150:151], v[2:3], v[176:177], v[150:151] op_sel_hi:[1,0,1]
	v_pk_mul_f32 v[146:147], v[146:147], v[180:181] op_sel_hi:[1,0]
	v_cvt_pk_fp8_f32 v159, v21, v23 op_sel:[0,0,1]
	v_pk_fma_f32 v[146:147], v[6:7], v[176:177], v[146:147] op_sel_hi:[1,0,1]
	v_med3_f32 v21, v150, s83, v173
	v_med3_f32 v23, v151, s83, v173
	v_mov_b32_e32 v150, 0
	v_cvt_pk_fp8_f32 v150, v21, v23
	v_med3_f32 v25, v146, s83, v173
	v_med3_f32 v27, v147, s83, v173
	v_mov_b32_e32 v151, 0
	v_pk_mul_f32 v[152:153], v[152:153], v[180:181] op_sel_hi:[1,0]
	v_cvt_pk_fp8_f32 v151, v25, v27
	v_pk_fma_f32 v[152:153], v[4:5], v[176:177], v[152:153] op_sel_hi:[1,0,1]
	v_pk_mul_f32 v[148:149], v[148:149], v[180:181] op_sel_hi:[1,0]
	v_med3_f32 v21, v152, s83, v173
	v_pk_fma_f32 v[148:149], v[8:9], v[176:177], v[148:149] op_sel_hi:[1,0,1]
	v_med3_f32 v23, v153, s83, v173
	s_or_b32 s27, s38, s66
	v_cvt_pk_fp8_f32 v150, v21, v23 op_sel:[0,0,1]
	v_med3_f32 v21, v148, s83, v173
	v_med3_f32 v23, v149, s83, v173
	v_add_u32_e32 v18, s27, v18
	v_cvt_pk_fp8_f32 v151, v21, v23 op_sel:[0,0,1]
	v_ashrrev_i32_e32 v19, 31, v18
	v_lshl_add_u64 v[146:147], s[10:11], 0, v[182:183]
	v_lshl_add_u64 v[146:147], v[146:147], 0, v[18:19]
	global_store_dwordx2 v[146:147], v[158:159], off
	global_store_dwordx2 v[146:147], v[150:151], off offset:128
	v_mul_f32_e32 v146, 0x3b800000, v178
	v_pk_mul_f32 v[142:143], v[142:143], v[146:147] op_sel_hi:[1,0]
	v_pk_mul_f32 v[138:139], v[138:139], v[146:147] op_sel_hi:[1,0]
	v_pk_fma_f32 v[142:143], v[10:11], v[178:179], v[142:143] op_sel_hi:[1,0,1]
	v_pk_fma_f32 v[138:139], v[14:15], v[178:179], v[138:139] op_sel_hi:[1,0,1]
	v_med3_f32 v21, v142, s83, v173
	v_med3_f32 v23, v143, s83, v173
	v_mov_b32_e32 v142, 0
	v_cvt_pk_fp8_f32 v142, v21, v23
	v_med3_f32 v25, v138, s83, v173
	v_med3_f32 v27, v139, s83, v173
	v_mov_b32_e32 v143, 0
	v_pk_mul_f32 v[144:145], v[144:145], v[146:147] op_sel_hi:[1,0]
	v_cvt_pk_fp8_f32 v143, v25, v27
	v_pk_fma_f32 v[144:145], v[12:13], v[178:179], v[144:145] op_sel_hi:[1,0,1]
	v_pk_mul_f32 v[140:141], v[140:141], v[146:147] op_sel_hi:[1,0]
	v_med3_f32 v21, v144, s83, v173
	v_pk_fma_f32 v[140:141], v[16:17], v[178:179], v[140:141] op_sel_hi:[1,0,1]
	v_med3_f32 v23, v145, s83, v173
	v_pk_mul_f32 v[134:135], v[134:135], v[146:147] op_sel_hi:[1,0]
	v_cvt_pk_fp8_f32 v142, v21, v23 op_sel:[0,0,1]
	v_med3_f32 v21, v140, s83, v173
	v_med3_f32 v23, v141, s83, v173
	v_pk_fma_f32 v[134:135], v[2:3], v[178:179], v[134:135] op_sel_hi:[1,0,1]
	v_pk_mul_f32 v[130:131], v[130:131], v[146:147] op_sel_hi:[1,0]
	v_cvt_pk_fp8_f32 v143, v21, v23 op_sel:[0,0,1]
	v_pk_fma_f32 v[130:131], v[6:7], v[178:179], v[130:131] op_sel_hi:[1,0,1]
	v_med3_f32 v21, v134, s83, v173
	v_med3_f32 v23, v135, s83, v173
	v_mov_b32_e32 v134, 0
	v_cvt_pk_fp8_f32 v134, v21, v23
	v_med3_f32 v25, v130, s83, v173
	v_med3_f32 v27, v131, s83, v173
	v_mov_b32_e32 v135, 0
	v_pk_mul_f32 v[136:137], v[136:137], v[146:147] op_sel_hi:[1,0]
	v_cvt_pk_fp8_f32 v135, v25, v27
	v_pk_fma_f32 v[136:137], v[4:5], v[178:179], v[136:137] op_sel_hi:[1,0,1]
	v_pk_mul_f32 v[132:133], v[132:133], v[146:147] op_sel_hi:[1,0]
	v_add_u32_e32 v148, 16, v22
	v_pk_fma_f32 v[132:133], v[8:9], v[178:179], v[132:133] op_sel_hi:[1,0,1]
	v_med3_f32 v21, v136, s83, v173
	v_med3_f32 v23, v137, s83, v173
	v_ashrrev_i32_e32 v149, 31, v148
	v_cvt_pk_fp8_f32 v134, v21, v23 op_sel:[0,0,1]
	v_med3_f32 v21, v132, s83, v173
	v_med3_f32 v23, v133, s83, v173
	v_lshlrev_b64 v[148:149], 10, v[148:149]
	v_cvt_pk_fp8_f32 v135, v21, v23 op_sel:[0,0,1]
	v_lshl_add_u64 v[130:131], s[10:11], 0, v[148:149]
	v_lshl_add_u64 v[130:131], v[130:131], 0, v[18:19]
	global_store_dwordx2 v[130:131], v[142:143], off
	global_store_dwordx2 v[130:131], v[134:135], off offset:128
	v_mul_f32_e32 v130, 0x3b800000, v32
	v_pk_mul_f32 v[126:127], v[126:127], v[130:131] op_sel_hi:[1,0]
	v_pk_mul_f32 v[122:123], v[122:123], v[130:131] op_sel_hi:[1,0]
	s_waitcnt lgkmcnt(0)
	v_pk_fma_f32 v[126:127], v[10:11], v[32:33], v[126:127] op_sel_hi:[1,0,1]
	v_pk_fma_f32 v[122:123], v[14:15], v[32:33], v[122:123] op_sel_hi:[1,0,1]
	v_med3_f32 v21, v126, s83, v173
	v_med3_f32 v23, v127, s83, v173
	v_mov_b32_e32 v126, 0
	v_cvt_pk_fp8_f32 v126, v21, v23
	v_med3_f32 v25, v122, s83, v173
	v_med3_f32 v27, v123, s83, v173
	v_mov_b32_e32 v127, 0
	v_pk_mul_f32 v[128:129], v[128:129], v[130:131] op_sel_hi:[1,0]
	v_cvt_pk_fp8_f32 v127, v25, v27
	v_pk_fma_f32 v[128:129], v[12:13], v[32:33], v[128:129] op_sel_hi:[1,0,1]
	v_pk_mul_f32 v[124:125], v[124:125], v[130:131] op_sel_hi:[1,0]
	v_cmp_gt_i32_e32 vcc, s26, v20
	v_add_u32_e32 v20, s17, v29
	v_pk_fma_f32 v[124:125], v[16:17], v[32:33], v[124:125] op_sel_hi:[1,0,1]
	v_med3_f32 v21, v128, s83, v173
	v_med3_f32 v23, v129, s83, v173
	v_pk_mul_f32 v[118:119], v[118:119], v[130:131] op_sel_hi:[1,0]
	v_cndmask_b32_e32 v24, 0, v31, vcc
	v_cmp_gt_i32_e32 vcc, s26, v20
	v_cvt_pk_fp8_f32 v126, v21, v23 op_sel:[0,0,1]
	v_med3_f32 v21, v124, s83, v173
	v_med3_f32 v23, v125, s83, v173
	v_pk_mul_f32 v[120:121], v[120:121], v[130:131] op_sel_hi:[1,0]
	v_pk_fma_f32 v[118:119], v[2:3], v[32:33], v[118:119] op_sel_hi:[1,0,1]
	v_pk_mul_f32 v[114:115], v[114:115], v[130:131] op_sel_hi:[1,0]
	v_pk_mul_f32 v[116:117], v[116:117], v[130:131] op_sel_hi:[1,0]
	v_cndmask_b32_e32 v20, 0, v33, vcc
	v_cvt_pk_fp8_f32 v127, v21, v23 op_sel:[0,0,1]
	v_pk_fma_f32 v[120:121], v[4:5], v[32:33], v[120:121] op_sel_hi:[1,0,1]
	v_pk_fma_f32 v[116:117], v[8:9], v[32:33], v[116:117] op_sel_hi:[1,0,1]
	v_pk_fma_f32 v[32:33], v[6:7], v[32:33], v[114:115] op_sel_hi:[1,0,1]
	v_med3_f32 v21, v118, s83, v173
	v_med3_f32 v23, v119, s83, v173
	v_mov_b32_e32 v114, 0
	v_cvt_pk_fp8_f32 v114, v21, v23
	v_med3_f32 v25, v32, s83, v173
	v_med3_f32 v27, v33, s83, v173
	v_mov_b32_e32 v115, 0
	v_cvt_pk_fp8_f32 v115, v25, v27
	v_add_u32_e32 v132, 32, v22
	v_med3_f32 v21, v120, s83, v173
	v_med3_f32 v23, v121, s83, v173
	v_ashrrev_i32_e32 v133, 31, v132
	v_cvt_pk_fp8_f32 v114, v21, v23 op_sel:[0,0,1]
	v_med3_f32 v21, v116, s83, v173
	v_med3_f32 v23, v117, s83, v173
	v_lshlrev_b64 v[132:133], 10, v[132:133]
	v_cvt_pk_fp8_f32 v115, v21, v23 op_sel:[0,0,1]
	v_lshl_add_u64 v[32:33], s[10:11], 0, v[132:133]
	v_lshl_add_u64 v[32:33], v[32:33], 0, v[18:19]
	global_store_dwordx2 v[32:33], v[126:127], off
	global_store_dwordx2 v[32:33], v[114:115], off offset:128
	v_mul_f32_e32 v32, 0x3b800000, v30
	v_pk_mul_f32 v[110:111], v[110:111], v[32:33] op_sel_hi:[1,0]
	v_pk_mul_f32 v[106:107], v[106:107], v[32:33] op_sel_hi:[1,0]
	v_pk_fma_f32 v[110:111], v[10:11], v[30:31], v[110:111] op_sel_hi:[1,0,1]
	v_pk_fma_f32 v[106:107], v[14:15], v[30:31], v[106:107] op_sel_hi:[1,0,1]
	v_med3_f32 v21, v110, s83, v173
	v_med3_f32 v23, v111, s83, v173
	v_mov_b32_e32 v110, 0
	v_cvt_pk_fp8_f32 v110, v21, v23
	v_med3_f32 v25, v106, s83, v173
	v_med3_f32 v27, v107, s83, v173
	v_mov_b32_e32 v111, 0
	v_pk_mul_f32 v[112:113], v[112:113], v[32:33] op_sel_hi:[1,0]
	v_cvt_pk_fp8_f32 v111, v25, v27
	v_pk_fma_f32 v[112:113], v[12:13], v[30:31], v[112:113] op_sel_hi:[1,0,1]
	v_pk_mul_f32 v[108:109], v[108:109], v[32:33] op_sel_hi:[1,0]
	v_med3_f32 v21, v112, s83, v173
	v_pk_fma_f32 v[108:109], v[16:17], v[30:31], v[108:109] op_sel_hi:[1,0,1]
	v_med3_f32 v23, v113, s83, v173
	v_pk_mul_f32 v[102:103], v[102:103], v[32:33] op_sel_hi:[1,0]
	v_cvt_pk_fp8_f32 v110, v21, v23 op_sel:[0,0,1]
	v_med3_f32 v21, v108, s83, v173
	v_med3_f32 v23, v109, s83, v173
	v_pk_mul_f32 v[104:105], v[104:105], v[32:33] op_sel_hi:[1,0]
	v_pk_fma_f32 v[102:103], v[2:3], v[30:31], v[102:103] op_sel_hi:[1,0,1]
	v_pk_mul_f32 v[98:99], v[98:99], v[32:33] op_sel_hi:[1,0]
	v_pk_mul_f32 v[32:33], v[100:101], v[32:33] op_sel_hi:[1,0]
	v_cvt_pk_fp8_f32 v111, v21, v23 op_sel:[0,0,1]
	v_pk_fma_f32 v[104:105], v[4:5], v[30:31], v[104:105] op_sel_hi:[1,0,1]
	v_pk_fma_f32 v[32:33], v[8:9], v[30:31], v[32:33] op_sel_hi:[1,0,1]
	v_pk_fma_f32 v[30:31], v[6:7], v[30:31], v[98:99] op_sel_hi:[1,0,1]
	v_med3_f32 v21, v102, s83, v173
	v_med3_f32 v23, v103, s83, v173
	v_mov_b32_e32 v98, 0
	v_cvt_pk_fp8_f32 v98, v21, v23
	v_med3_f32 v25, v30, s83, v173
	v_med3_f32 v27, v31, s83, v173
	v_mov_b32_e32 v99, 0
	v_med3_f32 v21, v104, s83, v173
	v_med3_f32 v23, v105, s83, v173
	v_cvt_pk_fp8_f32 v99, v25, v27
	v_cvt_pk_fp8_f32 v98, v21, v23 op_sel:[0,0,1]
	v_med3_f32 v21, v32, s83, v173
	v_mul_f32_e32 v32, 0x3b800000, v28
	v_pk_mul_f32 v[94:95], v[94:95], v[32:33] op_sel_hi:[1,0]
	v_med3_f32 v23, v33, s83, v173
	v_pk_fma_f32 v[94:95], v[10:11], v[28:29], v[94:95] op_sel_hi:[1,0,1]
	v_pk_mul_f32 v[90:91], v[90:91], v[32:33] op_sel_hi:[1,0]
	v_cvt_pk_fp8_f32 v99, v21, v23 op_sel:[0,0,1]
	v_pk_fma_f32 v[90:91], v[14:15], v[28:29], v[90:91] op_sel_hi:[1,0,1]
	v_med3_f32 v21, v94, s83, v173
	v_med3_f32 v23, v95, s83, v173
	v_mov_b32_e32 v94, 0
	v_cvt_pk_fp8_f32 v94, v21, v23
	v_med3_f32 v25, v90, s83, v173
	v_med3_f32 v27, v91, s83, v173
	v_mov_b32_e32 v95, 0
	v_pk_mul_f32 v[96:97], v[96:97], v[32:33] op_sel_hi:[1,0]
	v_cvt_pk_fp8_f32 v95, v25, v27
	v_pk_fma_f32 v[96:97], v[12:13], v[28:29], v[96:97] op_sel_hi:[1,0,1]
	v_pk_mul_f32 v[92:93], v[92:93], v[32:33] op_sel_hi:[1,0]
	v_med3_f32 v21, v96, s83, v173
	v_pk_fma_f32 v[92:93], v[16:17], v[28:29], v[92:93] op_sel_hi:[1,0,1]
	v_med3_f32 v23, v97, s83, v173
	v_pk_mul_f32 v[86:87], v[86:87], v[32:33] op_sel_hi:[1,0]
	v_add_u32_e32 v114, 48, v22
	v_cvt_pk_fp8_f32 v94, v21, v23 op_sel:[0,0,1]
	v_med3_f32 v21, v92, s83, v173
	v_med3_f32 v23, v93, s83, v173
	v_pk_mul_f32 v[88:89], v[88:89], v[32:33] op_sel_hi:[1,0]
	v_pk_fma_f32 v[86:87], v[2:3], v[28:29], v[86:87] op_sel_hi:[1,0,1]
	v_pk_mul_f32 v[82:83], v[82:83], v[32:33] op_sel_hi:[1,0]
	v_pk_mul_f32 v[32:33], v[84:85], v[32:33] op_sel_hi:[1,0]
	v_ashrrev_i32_e32 v115, 31, v114
	v_cvt_pk_fp8_f32 v95, v21, v23 op_sel:[0,0,1]
	v_pk_fma_f32 v[88:89], v[4:5], v[28:29], v[88:89] op_sel_hi:[1,0,1]
	v_pk_fma_f32 v[32:33], v[8:9], v[28:29], v[32:33] op_sel_hi:[1,0,1]
	v_pk_fma_f32 v[28:29], v[6:7], v[28:29], v[82:83] op_sel_hi:[1,0,1]
	v_med3_f32 v21, v86, s83, v173
	v_med3_f32 v23, v87, s83, v173
	v_mov_b32_e32 v82, 0
	v_lshlrev_b64 v[114:115], 10, v[114:115]
	v_cvt_pk_fp8_f32 v82, v21, v23
	v_med3_f32 v25, v28, s83, v173
	v_med3_f32 v27, v29, s83, v173
	v_mov_b32_e32 v83, 0
	v_lshl_add_u64 v[30:31], s[10:11], 0, v[114:115]
	v_cvt_pk_fp8_f32 v83, v25, v27
	v_lshl_add_u64 v[30:31], v[30:31], 0, v[18:19]
	global_store_dwordx2 v[30:31], v[110:111], off
	global_store_dwordx2 v[30:31], v[98:99], off offset:128
	v_add_u32_e32 v30, 0x80, v22
	v_med3_f32 v21, v88, s83, v173
	v_med3_f32 v23, v89, s83, v173
	v_ashrrev_i32_e32 v31, 31, v30
	v_cvt_pk_fp8_f32 v82, v21, v23 op_sel:[0,0,1]
	v_med3_f32 v21, v32, s83, v173
	v_med3_f32 v23, v33, s83, v173
	v_lshlrev_b64 v[30:31], 10, v[30:31]
	v_cvt_pk_fp8_f32 v83, v21, v23 op_sel:[0,0,1]
	v_lshl_add_u64 v[28:29], s[10:11], 0, v[30:31]
	v_lshl_add_u64 v[28:29], v[28:29], 0, v[18:19]
	global_store_dwordx2 v[28:29], v[94:95], off
	global_store_dwordx2 v[28:29], v[82:83], off offset:128
	v_mul_f32_e32 v28, 0x3b800000, v26
	v_pk_mul_f32 v[32:33], v[78:79], v[28:29] op_sel_hi:[1,0]
	v_pk_mul_f32 v[74:75], v[74:75], v[28:29] op_sel_hi:[1,0]
	v_pk_fma_f32 v[32:33], v[10:11], v[26:27], v[32:33] op_sel_hi:[1,0,1]
	v_pk_mul_f32 v[78:79], v[80:81], v[28:29] op_sel_hi:[1,0]
	v_pk_mul_f32 v[76:77], v[76:77], v[28:29] op_sel_hi:[1,0]
	v_pk_fma_f32 v[74:75], v[14:15], v[26:27], v[74:75] op_sel_hi:[1,0,1]
	v_med3_f32 v21, v32, s83, v173
	v_med3_f32 v23, v33, s83, v173
	v_mov_b32_e32 v32, 0
	v_pk_fma_f32 v[78:79], v[12:13], v[26:27], v[78:79] op_sel_hi:[1,0,1]
	v_pk_fma_f32 v[76:77], v[16:17], v[26:27], v[76:77] op_sel_hi:[1,0,1]
	v_cvt_pk_fp8_f32 v32, v21, v23
	v_med3_f32 v25, v74, s83, v173
	v_med3_f32 v27, v75, s83, v173
	v_mov_b32_e32 v33, 0
	v_cvt_pk_fp8_f32 v33, v25, v27
	v_med3_f32 v21, v78, s83, v173
	v_med3_f32 v23, v79, s83, v173
	v_pk_mul_f32 v[70:71], v[70:71], v[28:29] op_sel_hi:[1,0]
	v_cvt_pk_fp8_f32 v32, v21, v23 op_sel:[0,0,1]
	v_med3_f32 v21, v76, s83, v173
	v_med3_f32 v23, v77, s83, v173
	v_pk_mul_f32 v[72:73], v[72:73], v[28:29] op_sel_hi:[1,0]
	v_pk_fma_f32 v[70:71], v[2:3], v[26:27], v[70:71] op_sel_hi:[1,0,1]
	v_pk_mul_f32 v[66:67], v[66:67], v[28:29] op_sel_hi:[1,0]
	v_pk_mul_f32 v[28:29], v[68:69], v[28:29] op_sel_hi:[1,0]
	v_cvt_pk_fp8_f32 v33, v21, v23 op_sel:[0,0,1]
	v_pk_fma_f32 v[72:73], v[4:5], v[26:27], v[72:73] op_sel_hi:[1,0,1]
	v_pk_fma_f32 v[28:29], v[8:9], v[26:27], v[28:29] op_sel_hi:[1,0,1]
	v_pk_fma_f32 v[26:27], v[6:7], v[26:27], v[66:67] op_sel_hi:[1,0,1]
	v_med3_f32 v21, v70, s83, v173
	v_med3_f32 v23, v71, s83, v173
	v_mov_b32_e32 v66, 0
	v_cvt_pk_fp8_f32 v66, v21, v23
	v_med3_f32 v25, v26, s83, v173
	v_med3_f32 v26, v27, s83, v173
	v_mov_b32_e32 v67, 0
	v_cvt_pk_fp8_f32 v67, v25, v26
	v_add_u32_e32 v30, 0x90, v22
	v_med3_f32 v21, v72, s83, v173
	v_med3_f32 v23, v73, s83, v173
	v_ashrrev_i32_e32 v31, 31, v30
	v_cvt_pk_fp8_f32 v66, v21, v23 op_sel:[0,0,1]
	v_med3_f32 v21, v28, s83, v173
	v_med3_f32 v23, v29, s83, v173
	v_lshlrev_b64 v[30:31], 10, v[30:31]
	v_cvt_pk_fp8_f32 v67, v21, v23 op_sel:[0,0,1]
	v_lshl_add_u64 v[26:27], s[10:11], 0, v[30:31]
	v_lshl_add_u64 v[26:27], v[26:27], 0, v[18:19]
	global_store_dwordx2 v[26:27], v[32:33], off
	global_store_dwordx2 v[26:27], v[66:67], off offset:128
	v_mul_f32_e32 v26, 0x3b800000, v24
	v_pk_mul_f32 v[30:31], v[62:63], v[26:27] op_sel_hi:[1,0]
	v_pk_mul_f32 v[58:59], v[58:59], v[26:27] op_sel_hi:[1,0]
	v_pk_fma_f32 v[30:31], v[10:11], v[24:25], v[30:31] op_sel_hi:[1,0,1]
	v_pk_mul_f32 v[32:33], v[64:65], v[26:27] op_sel_hi:[1,0]
	v_pk_mul_f32 v[60:61], v[60:61], v[26:27] op_sel_hi:[1,0]
	v_pk_fma_f32 v[58:59], v[14:15], v[24:25], v[58:59] op_sel_hi:[1,0,1]
	v_med3_f32 v21, v30, s83, v173
	v_med3_f32 v23, v31, s83, v173
	v_mov_b32_e32 v30, 0
	v_pk_fma_f32 v[32:33], v[12:13], v[24:25], v[32:33] op_sel_hi:[1,0,1]
	v_pk_fma_f32 v[60:61], v[16:17], v[24:25], v[60:61] op_sel_hi:[1,0,1]
	v_cvt_pk_fp8_f32 v30, v21, v23
	v_med3_f32 v25, v58, s83, v173
	v_med3_f32 v27, v59, s83, v173
	v_mov_b32_e32 v31, 0
	v_cvt_pk_fp8_f32 v31, v25, v27
	v_med3_f32 v21, v32, s83, v173
	v_med3_f32 v23, v33, s83, v173
	v_pk_mul_f32 v[32:33], v[54:55], v[26:27] op_sel_hi:[1,0]
	v_cvt_pk_fp8_f32 v30, v21, v23 op_sel:[0,0,1]
	v_med3_f32 v21, v60, s83, v173
	v_med3_f32 v23, v61, s83, v173
	v_pk_mul_f32 v[54:55], v[56:57], v[26:27] op_sel_hi:[1,0]
	v_pk_fma_f32 v[32:33], v[2:3], v[24:25], v[32:33] op_sel_hi:[1,0,1]
	v_pk_mul_f32 v[50:51], v[50:51], v[26:27] op_sel_hi:[1,0]
	v_pk_mul_f32 v[26:27], v[52:53], v[26:27] op_sel_hi:[1,0]
	v_cvt_pk_fp8_f32 v31, v21, v23 op_sel:[0,0,1]
	v_pk_fma_f32 v[54:55], v[4:5], v[24:25], v[54:55] op_sel_hi:[1,0,1]
	v_pk_fma_f32 v[26:27], v[8:9], v[24:25], v[26:27] op_sel_hi:[1,0,1]
	v_pk_fma_f32 v[24:25], v[6:7], v[24:25], v[50:51] op_sel_hi:[1,0,1]
	v_med3_f32 v21, v32, s83, v173
	v_med3_f32 v23, v33, s83, v173
	v_mov_b32_e32 v32, 0
	v_cvt_pk_fp8_f32 v32, v21, v23
	v_med3_f32 v24, v24, s83, v173
	v_med3_f32 v25, v25, s83, v173
	v_mov_b32_e32 v33, 0
	v_cvt_pk_fp8_f32 v33, v24, v25
	v_add_u32_e32 v28, 0xa0, v22
	v_med3_f32 v21, v54, s83, v173
	v_med3_f32 v23, v55, s83, v173
	v_ashrrev_i32_e32 v29, 31, v28
	v_cvt_pk_fp8_f32 v32, v21, v23 op_sel:[0,0,1]
	v_med3_f32 v21, v26, s83, v173
	v_med3_f32 v23, v27, s83, v173
	v_lshlrev_b64 v[28:29], 10, v[28:29]
	v_cvt_pk_fp8_f32 v33, v21, v23 op_sel:[0,0,1]
	v_lshl_add_u64 v[24:25], s[10:11], 0, v[28:29]
	v_lshl_add_u64 v[24:25], v[24:25], 0, v[18:19]
	global_store_dwordx2 v[24:25], v[30:31], off
	global_store_dwordx2 v[24:25], v[32:33], off offset:128
	v_mul_f32_e32 v24, 0x3b800000, v20
	v_pk_mul_f32 v[26:27], v[46:47], v[24:25] op_sel_hi:[1,0]
	v_pk_mul_f32 v[28:29], v[48:49], v[24:25] op_sel_hi:[1,0]
	v_pk_fma_f32 v[10:11], v[10:11], v[20:21], v[26:27] op_sel_hi:[1,0,1]
	v_pk_fma_f32 v[12:13], v[12:13], v[20:21], v[28:29] op_sel_hi:[1,0,1]
	v_pk_mul_f32 v[26:27], v[42:43], v[24:25] op_sel_hi:[1,0]
	v_pk_mul_f32 v[28:29], v[44:45], v[24:25] op_sel_hi:[1,0]
	v_pk_fma_f32 v[14:15], v[14:15], v[20:21], v[26:27] op_sel_hi:[1,0,1]
	v_pk_fma_f32 v[16:17], v[16:17], v[20:21], v[28:29] op_sel_hi:[1,0,1]
	v_med3_f32 v21, v10, s83, v173
	v_med3_f32 v11, v11, s83, v173
	v_mov_b32_e32 v10, 0
	v_cvt_pk_fp8_f32 v10, v21, v11
	v_med3_f32 v14, v14, s83, v173
	v_med3_f32 v15, v15, s83, v173
	v_mov_b32_e32 v11, 0
	v_cvt_pk_fp8_f32 v11, v14, v15
	v_med3_f32 v12, v12, s83, v173
	v_med3_f32 v13, v13, s83, v173
	v_cvt_pk_fp8_f32 v10, v12, v13 op_sel:[0,0,1]
	v_med3_f32 v12, v16, s83, v173
	v_med3_f32 v13, v17, s83, v173
	v_cvt_pk_fp8_f32 v11, v12, v13 op_sel:[0,0,1]
	v_pk_mul_f32 v[12:13], v[38:39], v[24:25] op_sel_hi:[1,0]
	v_pk_mul_f32 v[14:15], v[40:41], v[24:25] op_sel_hi:[1,0]
	v_pk_fma_f32 v[2:3], v[2:3], v[20:21], v[12:13] op_sel_hi:[1,0,1]
	v_pk_mul_f32 v[12:13], v[34:35], v[24:25] op_sel_hi:[1,0]
	v_med3_f32 v3, v3, s83, v173
	v_pk_fma_f32 v[6:7], v[6:7], v[20:21], v[12:13] op_sel_hi:[1,0,1]
	v_med3_f32 v12, v2, s83, v173
	v_mov_b32_e32 v2, 0
	v_cvt_pk_fp8_f32 v2, v12, v3
	v_med3_f32 v6, v6, s83, v173
	v_med3_f32 v7, v7, s83, v173
	v_mov_b32_e32 v3, 0
	v_cvt_pk_fp8_f32 v3, v6, v7
	v_pk_fma_f32 v[4:5], v[4:5], v[20:21], v[14:15] op_sel_hi:[1,0,1]
	v_pk_mul_f32 v[14:15], v[36:37], v[24:25] op_sel_hi:[1,0]
	v_add_u32_e32 v22, 0xb0, v22
	v_pk_fma_f32 v[8:9], v[8:9], v[20:21], v[14:15] op_sel_hi:[1,0,1]
	v_med3_f32 v4, v4, s83, v173
	v_med3_f32 v5, v5, s83, v173
	v_ashrrev_i32_e32 v23, 31, v22
	v_cvt_pk_fp8_f32 v2, v4, v5 op_sel:[0,0,1]
	v_med3_f32 v4, v8, s83, v173
	v_med3_f32 v5, v9, s83, v173
	v_lshlrev_b64 v[22:23], 10, v[22:23]
	v_cvt_pk_fp8_f32 v3, v4, v5 op_sel:[0,0,1]
	v_lshl_add_u64 v[4:5], s[10:11], 0, v[22:23]
	v_lshl_add_u64 v[4:5], v[4:5], 0, v[18:19]
	s_and_b64 vcc, exec, s[6:7]
	s_mov_b64 s[6:7], -1
	v_readlane_b32 s90, v253, 26
	global_store_dwordx2 v[4:5], v[10:11], off
	global_store_dwordx2 v[4:5], v[2:3], off offset:128
	s_cbranch_vccnz .LBB0_2057
	s_andn2_b64 vcc, exec, s[8:9]
	s_cbranch_vccnz .LBB0_2056
	s_barrier
	s_branch .LBB0_2056
